# adds pseudo-random first-round start delay in k_upsample (z<2) on top of v46
# baseline (speedup 1.0000x reference)
_Z10k_upsamplePKfS0_PfS1_:
	s_cmp_lt_u32 s4, 2
	s_cbranch_scc0 .Lup_nosleep
	s_getreg_b32 s16, hwreg(HW_REG_HW_ID, 0, 20)
	s_mul_i32 s16, s16, 0x9e3b
	s_lshr_b32 s16, s16, 9
	s_and_b32 s16, s16, 15
	s_cmp_eq_u32 s16, 0
	s_cbranch_scc1 .Lup_nosleep
.Lup_sleep:
	s_sleep 4
	s_add_i32 s16, s16, -1
	s_cmp_lg_u32 s16, 0
	s_cbranch_scc1 .Lup_sleep
.Lup_nosleep:
	s_ashr_i32 s5, s4, 31
	s_load_dwordx4 s[8:11], s[0:1], 0x0
	s_load_dwordx2 s[6:7], s[0:1], 0x10
	s_lshl_b64 s[12:13], s[4:5], 6
	s_ashr_i32 s5, s3, 31
	v_lshrrev_b32_e32 v1, 6, v0
	s_add_u32 s12, s12, s3
	v_lshl_or_b32 v19, s2, 2, v1
	s_addc_u32 s13, s13, s5
	v_and_b32_e32 v29, 63, v0
	s_lshl_b64 s[14:15], s[12:13], 14
	v_max_i32_e32 v2, 1, v19
	v_not_b32_e32 v3, 63
	s_waitcnt lgkmcnt(0)
	s_add_u32 s8, s8, s14
	v_sub_u32_e64 v14, v29, 1 clamp
	v_lshl_add_u32 v8, v2, 6, v3
	s_addc_u32 s9, s9, s15
	v_min_i32_e32 v15, 62, v19
	v_or_b32_e32 v2, v14, v8
	v_mov_b32_e32 v3, 0
	v_min_u32_e32 v21, 62, v29
	v_lshl_add_u64 v[4:5], v[2:3], 2, s[8:9]
	v_or_b32_e32 v2, v8, v29
	v_lshlrev_b32_e32 v12, 6, v19
	v_lshl_add_u32 v23, v15, 6, 64
	v_lshl_add_u64 v[6:7], v[2:3], 2, s[8:9]
	v_or_b32_e32 v2, v21, v8
	v_or_b32_e32 v8, v14, v12
	v_or_b32_e32 v10, v12, v29
	v_or_b32_e32 v14, v14, v23
	v_or_b32_e32 v16, v23, v29
	v_lshl_add_u64 v[2:3], v[2:3], 2, s[8:9]
	v_ashrrev_i32_e32 v9, 31, v8
	v_ashrrev_i32_e32 v11, 31, v10
	v_ashrrev_i32_e32 v13, 31, v12
	v_or_b32_e32 v12, v12, v21
	v_ashrrev_i32_e32 v15, 31, v14
	v_ashrrev_i32_e32 v17, 31, v16
	v_lshl_add_u64 v[8:9], v[8:9], 2, s[8:9]
	v_lshl_add_u64 v[10:11], v[10:11], 2, s[8:9]
	v_lshl_add_u64 v[12:13], v[12:13], 2, s[8:9]
	v_lshl_add_u64 v[14:15], v[14:15], 2, s[8:9]
	v_lshl_add_u64 v[16:17], v[16:17], 2, s[8:9]
	global_load_dword v18, v[4:5], off
	global_load_dword v20, v[6:7], off
	global_load_dword v25, v[2:3], off offset:4
	global_load_dword v22, v[8:9], off
	global_load_dword v24, v[10:11], off
	global_load_dword v27, v[12:13], off offset:4
	global_load_dword v26, v[14:15], off
	global_load_dword v28, v[16:17], off
	v_ashrrev_i32_e32 v3, 31, v23
	v_or_b32_e32 v2, v23, v21
	v_lshl_add_u64 v[2:3], v[2:3], 2, s[8:9]
	global_load_dword v21, v[2:3], off offset:4
	v_lshlrev_b32_e32 v2, 2, v19
	v_ashrrev_i32_e32 v3, 31, v2
	s_lshl_b64 s[8:9], s[12:13], 16
	v_lshlrev_b64 v[2:3], 8, v[2:3]
	v_lshl_add_u64 v[2:3], v[2:3], 0, s[8:9]
	v_lshl_or_b32 v2, v29, 2, v2
	v_lshlrev_b64 v[30:31], 2, v[2:3]
	v_lshl_add_u64 v[32:33], s[10:11], 0, v[30:31]
	global_load_dwordx4 v[2:5], v[32:33], off
	global_load_dwordx4 v[6:9], v[32:33], off offset:1024
	global_load_dwordx4 v[10:13], v[32:33], off offset:2048
	global_load_dwordx4 v[14:17], v[32:33], off offset:3072
	s_mov_b32 s8, 0x3f200000
	s_mov_b32 s9, 0x3f600000
	s_mov_b32 s10, 0x3e000000
	s_mov_b32 s11, 0x3ec00000
	s_mov_b32 s12, s9
	s_waitcnt vmcnt(11)
	v_sub_f32_e32 v32, v20, v18
	v_pk_fma_f32 v[32:33], v[32:33], s[8:9], v[18:19] op_sel_hi:[0,1,0]
	s_waitcnt vmcnt(10)
	v_sub_f32_e32 v34, v25, v20
	s_waitcnt vmcnt(8)
	v_sub_f32_e32 v36, v24, v22
	v_pk_fma_f32 v[36:37], v[36:37], s[8:9], v[22:23] op_sel_hi:[0,1,0]
	s_waitcnt vmcnt(7)
	v_sub_f32_e32 v38, v27, v24
	v_pk_add_f32 v[22:23], v[36:37], v[32:33] neg_lo:[0,1] neg_hi:[0,1]
	v_pk_fma_f32 v[38:39], v[38:39], s[10:11], v[24:25] op_sel_hi:[0,1,0]
	v_pk_fma_f32 v[18:19], v[22:23], s[8:9], v[32:33] op_sel_hi:[1,0,1]
	v_pk_fma_f32 v[22:23], v[22:23], s[12:13], v[32:33] op_sel_hi:[1,0,1]
	s_waitcnt vmcnt(4)
	v_pk_fma_f32 v[34:35], v[34:35], s[10:11], v[20:21] op_sel_hi:[0,1,0]
	v_pk_add_f32 v[24:25], v[38:39], v[34:35] neg_lo:[0,1] neg_hi:[0,1]
	v_sub_f32_e32 v42, v21, v28
	v_pk_fma_f32 v[20:21], v[24:25], s[8:9], v[34:35] op_sel_hi:[1,0,1]
	v_pk_fma_f32 v[24:25], v[24:25], s[12:13], v[34:35] op_sel_hi:[1,0,1]
	v_sub_f32_e32 v40, v28, v26
	s_waitcnt vmcnt(3)
	v_sub_f32_e32 v3, v19, v3
	v_sub_f32_e32 v2, v18, v2
	v_mul_f32_e32 v3, v3, v3
	v_sub_f32_e32 v4, v20, v4
	v_fmac_f32_e32 v3, v2, v2
	v_fmac_f32_e32 v3, v4, v4
	s_waitcnt vmcnt(2)
	v_sub_f32_e32 v4, v23, v7
	v_sub_f32_e32 v5, v21, v5
	v_sub_f32_e32 v2, v22, v6
	v_mul_f32_e32 v4, v4, v4
	v_fmac_f32_e32 v3, v5, v5
	v_sub_f32_e32 v5, v24, v8
	v_fmac_f32_e32 v4, v2, v2
	v_sub_f32_e32 v6, v25, v9
	v_fmac_f32_e32 v4, v5, v5
	v_fmac_f32_e32 v4, v6, v6
	v_add_f32_e32 v8, v3, v4
	v_pk_fma_f32 v[2:3], v[40:41], s[8:9], v[26:27] op_sel_hi:[0,1,0]
	v_pk_add_f32 v[2:3], v[2:3], v[36:37] neg_lo:[0,1] neg_hi:[0,1]
	v_pk_fma_f32 v[6:7], v[42:43], s[10:11], v[28:29] op_sel_hi:[0,1,0]
	v_pk_fma_f32 v[4:5], v[2:3], s[10:11], v[36:37] op_sel_hi:[1,0,1]
	v_pk_add_f32 v[26:27], v[6:7], v[38:39] neg_lo:[0,1] neg_hi:[0,1]
	s_waitcnt vmcnt(1)
	v_sub_f32_e32 v9, v4, v10
	v_sub_f32_e32 v10, v5, v11
	v_pk_fma_f32 v[6:7], v[26:27], s[10:11], v[38:39] op_sel_hi:[1,0,1]
	v_mul_f32_e32 v10, v10, v10
	v_sub_f32_e32 v11, v6, v12
	v_fmac_f32_e32 v10, v9, v9
	v_sub_f32_e32 v12, v7, v13
	v_fmac_f32_e32 v10, v11, v11
	v_fmac_f32_e32 v10, v12, v12
	s_mov_b32 s8, s11
	v_add_f32_e32 v12, v8, v10
	v_pk_fma_f32 v[8:9], v[2:3], s[8:9], v[36:37] op_sel_hi:[1,0,1]
	v_pk_fma_f32 v[10:11], v[26:27], s[8:9], v[38:39] op_sel_hi:[1,0,1]
	s_waitcnt vmcnt(0)
	v_sub_f32_e32 v3, v9, v15
	v_sub_f32_e32 v2, v8, v14
	v_mul_f32_e32 v3, v3, v3
	v_sub_f32_e32 v13, v10, v16
	v_fmac_f32_e32 v3, v2, v2
	v_sub_f32_e32 v14, v11, v17
	v_fmac_f32_e32 v3, v13, v13
	v_fmac_f32_e32 v3, v14, v14
	v_add_f32_e32 v2, v12, v3
	v_mbcnt_lo_u32_b32 v3, -1, 0
	v_mbcnt_hi_u32_b32 v3, -1, v3
	v_and_b32_e32 v12, 64, v3
	v_add_u32_e32 v14, 64, v12
	v_xor_b32_e32 v12, 32, v3
	v_cmp_lt_i32_e32 vcc, v12, v14
	s_nop 1
	v_cndmask_b32_e32 v12, v3, v12, vcc
	v_lshlrev_b32_e32 v12, 2, v12
	ds_bpermute_b32 v12, v12, v2
	s_waitcnt lgkmcnt(0)
	v_add_f32_e32 v2, v2, v12
	v_xor_b32_e32 v12, 16, v3
	v_cmp_lt_i32_e32 vcc, v12, v14
	s_nop 1
	v_cndmask_b32_e32 v12, v3, v12, vcc
	v_lshlrev_b32_e32 v12, 2, v12
	ds_bpermute_b32 v12, v12, v2
	s_waitcnt lgkmcnt(0)
	v_add_f32_e32 v2, v2, v12
	v_xor_b32_e32 v12, 8, v3
	v_cmp_lt_i32_e32 vcc, v12, v14
	s_nop 1
	v_cndmask_b32_e32 v12, v3, v12, vcc
	v_lshlrev_b32_e32 v12, 2, v12
	ds_bpermute_b32 v12, v12, v2
	s_waitcnt lgkmcnt(0)
	v_add_f32_e32 v2, v2, v12
	v_xor_b32_e32 v12, 4, v3
	v_cmp_lt_i32_e32 vcc, v12, v14
	s_nop 1
	v_cndmask_b32_e32 v12, v3, v12, vcc
	v_lshlrev_b32_e32 v12, 2, v12
	ds_bpermute_b32 v12, v12, v2
	s_waitcnt lgkmcnt(0)
	v_add_f32_e32 v2, v2, v12
	v_xor_b32_e32 v12, 2, v3
	v_cmp_lt_i32_e32 vcc, v12, v14
	s_nop 1
	v_cndmask_b32_e32 v12, v3, v12, vcc
	v_lshlrev_b32_e32 v12, 2, v12
	ds_bpermute_b32 v15, v12, v2
	v_lshl_add_u64 v[12:13], s[6:7], 0, v[30:31]
	global_store_dwordx4 v[12:13], v[18:21], off
	global_store_dwordx4 v[12:13], v[22:25], off offset:1024
	global_store_dwordx4 v[12:13], v[4:7], off offset:2048
	global_store_dwordx4 v[12:13], v[8:11], off offset:3072
	s_waitcnt lgkmcnt(0)
	v_add_f32_e32 v2, v2, v15
	v_xor_b32_e32 v15, 1, v3
	v_cmp_lt_i32_e32 vcc, v15, v14
	s_nop 1
	v_cndmask_b32_e32 v3, v3, v15, vcc
	v_lshlrev_b32_e32 v3, 2, v3
	ds_bpermute_b32 v3, v3, v2
	v_cmp_eq_u32_e32 vcc, 0, v29
	s_and_saveexec_b64 s[6:7], vcc
	s_cbranch_execz .LBB2_2
	s_waitcnt lgkmcnt(0)
	v_add_f32_e32 v2, v2, v3
	v_lshlrev_b32_e32 v1, 2, v1
	ds_write_b32 v1, v2

	.amdhsa_kernel _Z10k_upsamplePKfS0_PfS1_
		.amdhsa_group_segment_fixed_size 16
		.amdhsa_private_segment_fixed_size 0
		.amdhsa_kernarg_size 288
		.amdhsa_user_sgpr_count 2
		.amdhsa_user_sgpr_dispatch_ptr 0
		.amdhsa_user_sgpr_queue_ptr 0
		.amdhsa_user_sgpr_kernarg_segment_ptr 1
		.amdhsa_user_sgpr_dispatch_id 0
		.amdhsa_user_sgpr_kernarg_preload_length 0
		.amdhsa_user_sgpr_kernarg_preload_offset 0
		.amdhsa_user_sgpr_private_segment_size 0
		.amdhsa_uses_dynamic_stack 0
		.amdhsa_enable_private_segment 0
		.amdhsa_system_sgpr_workgroup_id_x 1
		.amdhsa_system_sgpr_workgroup_id_y 1
		.amdhsa_system_sgpr_workgroup_id_z 1
		.amdhsa_system_sgpr_workgroup_info 0
		.amdhsa_system_vgpr_workitem_id 0
		.amdhsa_next_free_vgpr 44
		.amdhsa_next_free_sgpr 24
		.amdhsa_accum_offset 44
		.amdhsa_reserve_vcc 1
		.amdhsa_float_round_mode_32 0
		.amdhsa_float_round_mode_16_64 0
		.amdhsa_float_denorm_mode_32 3
		.amdhsa_float_denorm_mode_16_64 3
		.amdhsa_dx10_clamp 1
		.amdhsa_ieee_mode 1
		.amdhsa_fp16_overflow 0
		.amdhsa_tg_split 0
		.amdhsa_exception_fp_ieee_invalid_op 0
		.amdhsa_exception_fp_denorm_src 0
		.amdhsa_exception_fp_ieee_div_zero 0
		.amdhsa_exception_fp_ieee_overflow 0
		.amdhsa_exception_fp_ieee_underflow 0
		.amdhsa_exception_fp_ieee_inexact 0
		.amdhsa_exception_int_div_zero 0
	.end_amdhsa_kernel
